# P0 static strip walk: second-round strips spread one or two per workgroup
# speedup vs baseline: 1.0021x; 1.0021x over previous
; #define P0_GET() do { if (DYN) { int v_ = 0x7fffffff; if (lane == 0) { if (!check_stop || __hip_atomic_load(stopw, RLX_AGENT) == 0u) v_ = (int)atomicAdd(qword, 1u); } \
;         idx = __builtin_amdgcn_readfirstlane(v_); ok = idx < P0_NHALF; } else { idx = cur_static; cur_static += nw; ok = idx < s1; } } while (0)
; #define P0_MAKE() (DYN ? p0_strip_half(args, ws, idx) : p0_strip(args, ws, idx))
; __device__ __forceinline__ Strip p0_strip(const Args& args, unsigned char* ws, int s) {
;     ...
;     s -= 6144;
;     int nseg, K, N; size_t wsoff; int in_idx;
;     if (s < 1032)                  { in_idx = I_W_IN;       K = 2048; N = 8256; nseg = 4; wsoff = WS_WIN;  st.mode = 1; st.out8 = 1; }
;     else if ((s -= 1032) < 48)     { in_idx = I_W_UQ;       K = 512;  N = 1536; nseg = 1; wsoff = WS_WUQ;  st.mode = 2; st.out8 = 0; }
;     else if ((s -= 48) < 64)       { in_idx = I_W_UKV;      K = 512;  N = 2048; nseg = 1; wsoff = WS_WUKV; st.mode = 0; st.out8 = 0; }
;     else if ((s -= 64) < 128)      { in_idx = I_W_O_MLA;    K = 1024; N = 2048; nseg = 2; wsoff = WS_WOA;  st.mode = 0; st.out8 = 1; }
;     else if ((s -= 128) < 128)     { in_idx = I_W_O_MOBA;   K = 1024; N = 2048; nseg = 2; wsoff = WS_WOB;  st.mode = 0; st.out8 = 1; }
;     else if ((s -= 128) < 256)     { in_idx = I_W_OUT;      K = 2048; N = 2048; nseg = 4; wsoff = WS_WOUT; st.mode = 0; st.out8 = 1; }
;     else if ((s -= 256) < 256)     { in_idx = I_W_PLE_GATE; K = 2048; N = 2048; nseg = 4; wsoff = WS_WPG;  st.mode = 0; st.out8 = 1; }
;     else { s -= 256;                 in_idx = I_W_PLE;      K = 256;  N = 2048; nseg = 1; wsoff = WS_WPLE; st.mode = 0; st.out8 = 0; }
;     const int nb = s / nseg, seg = s % nseg, nkt = K / 64, nk = nkt / nseg, kbeg = seg * nk * 64;
; template <bool DYN>
; __device__ __forceinline__ void p0_walk(const Args& args, unsigned char* ws, LAS float* scr, int lane, int w, int nw, int s0, int s1, unsigned* qword, unsigned* stopw, bool check_stop) {
;     int cur_static = s0 + w, idx = 0; bool ok = false;
;     ...
;     P0_GET();
;     if (!ok) return;
;     Strip lst = P0_MAKE(), sst = lst, nst = lst; bool has_n = false, lv = true, sv = true; int lj = 0, sj = 0;
.LBB0_328:
	s_and_b64 vcc, exec, s[6:7]
	v_writelane_b32 v252, s92, 4
	s_nop 1
	v_writelane_b32 v252, s93, 5
	s_cbranch_vccz .LBB0_1373
	s_sub_i32 s86, s2, s87
	s_add_u32 s38, s18, 0x100000
	s_addc_u32 s39, s19, 0
	s_cmp_lt_i32 s20, 1
	s_cselect_b64 s[4:5], -1, 0
	s_cmp_gt_i32 s21, 0
	s_cselect_b64 s[6:7], -1, 0
	s_and_b64 s[40:41], s[4:5], s[6:7]
	s_andn2_b64 vcc, exec, s[40:41]
	s_cbranch_vccnz .LBB0_1104
	s_lshl_b32 s3, s86, 3
	s_add_i32 s42, s3, s74
	s_lshl_b32 s44, s85, 3
	s_and_b64 s[4:5], s[34:35], exec
	s_cselect_b32 s3, 0x1800, 0
	s_mul_i32 s98, s74, s85
	s_add_i32 s98, s98, s86
	s_add_i32 s3, s98, s3
	s_cmpk_gt_i32 s3, 0x1fb7
	s_cbranch_scc1 .LBB0_1088
	s_load_dwordx2 s[48:49], s[0:1], 0x88
	s_load_dwordx4 s[8:11], s[0:1], 0x20
	s_load_dwordx2 s[50:51], s[0:1], 0x78
	s_add_u32 s43, s18, 0x3700400
	s_addc_u32 s45, s19, 0
	s_cmpk_gt_i32 s3, 0x17ff
	s_cbranch_scc0 .LBB0_339
	s_cmpk_lt_u32 s3, 0x1c08
	s_mov_b64 s[6:7], 0
	s_cbranch_scc1 .LBB0_340
	s_cmpk_lt_u32 s3, 0x1c38
	s_cbranch_scc1 .LBB0_341
	s_cmpk_lt_u32 s3, 0x1c78
	s_cbranch_scc1 .LBB0_342
	s_cmpk_lt_u32 s3, 0x1cf8
	s_mov_b64 s[52:53], 0
	s_cbranch_scc1 .LBB0_343
	s_cmpk_lt_u32 s3, 0x1d78
	s_cbranch_scc1 .LBB0_344
	s_cmpk_lt_u32 s3, 0x1e78
	s_cbranch_scc1 .LBB0_345
	s_cmpk_gt_u32 s3, 0x1f77
	s_cselect_b64 s[60:61], -1, 0
	s_cmpk_lt_u32 s3, 0x1f78
	s_cselect_b64 s[26:27], -1, 0
	s_and_b64 s[4:5], s[60:61], exec
	s_movk_i32 s16, 0xe088
	s_movk_i32 s5, 0x100
	s_mov_b32 s17, 0x4f00000
	s_cselect_b32 s4, s16, 0xffffe188
	s_cselect_b32 s16, 1, 4
	s_cselect_b32 s5, s5, 0x800
	s_cselect_b32 s58, s17, 0x4700000
	s_mov_b32 s59, 0
	s_cselect_b32 s56, 23, 22
	v_cndmask_b32_e64 v165, 0, 1, s[26:27]
	s_branch .LBB0_346

; __device__ __forceinline__ Strip p0_strip(const Args& args, unsigned char* ws, int s) {
;     ...
;     if (s < 6144) { const int mi = s >> 6, nb = s & 63, which = mi >> 5, e = mi & 31;
;         st.ldw = 2048; st.Kb = 2048; st.nk = 32; st.out8 = 1; st.n0 = nb * 32;
;         if (which == 0) { st.src = args.in[I_W_GATE] + (size_t)e * DM * DM; st.dst = ws + WS_WGU + (size_t)e * 4096 * 2048; st.mode = 3; }
;         else if (which == 1) { st.src = args.in[I_W_UP] + (size_t)e * DM * DM; st.dst = ws + WS_WGU + (size_t)e * 4096 * 2048; st.mode = 4; }
;         else { st.src = args.in[I_W_DOWN] + (size_t)e * DM * DM; st.dst = ws + WS_WDN + (size_t)e * 2048 * 2048; st.mode = 0; }
;         st.src += st.n0; return st; }
.LBB0_350:
	s_load_dwordx2 s[22:23], s[0:1], 0x98
	s_bfe_u32 s5, s98, 0x50006
	s_lshl_b32 s4, s98, 5
	s_and_b32 s4, s4, 0x7e0
	s_and_b32 s6, s3, 0xfffff800
	s_lshl_b32 s7, s5, 22
	s_lshl_b32 s16, s5, 24
	s_waitcnt lgkmcnt(0)
	s_add_u32 s17, s22, s16
	s_addc_u32 s22, s23, 0
	v_readlane_b32 s23, v252, 3
	s_add_u32 s7, s23, s7
	s_addc_u32 s23, s84, 0
	s_add_u32 s26, s48, s16
	s_addc_u32 s27, s49, 0
	s_lshl_b32 s5, s5, 23
	s_add_u32 s5, s80, s5
	s_addc_u32 s46, s81, 0
	s_add_u32 s16, s50, s16
	s_addc_u32 s47, s51, 0
	s_cmpk_eq_i32 s6, 0x800
	s_cselect_b32 s17, s26, s17
	s_cselect_b32 s22, s27, s22
	s_cselect_b32 s26, 4, 0
	s_cmpk_lt_u32 s3, 0x1000
	s_cselect_b32 s6, s5, s7
	s_cselect_b32 s7, s46, s23
	s_cmpk_lt_u32 s3, 0x800
	s_cselect_b32 s5, s47, s22
	s_cselect_b32 s16, s16, s17
	s_cselect_b32 s88, 3, s26
	s_lshl_b32 s17, s4, 2
	s_add_u32 s56, s16, s17
	s_movk_i32 s54, 0x800
	s_addc_u32 s57, s5, 0
	s_mov_b64 s[52:53], 0
	s_mov_b32 s46, 32
	v_mov_b32_e32 v167, 0x800
	v_mov_b64_e32 v[138:139], s[6:7]
	v_mov_b32_e32 v165, 1
